# baseline (speedup 1.0000x reference)
.Lp4_last:
	s_lshl_b32 s48, s17, 18
	s_or_b32 s49, s49, s48
	s_mov_b32 m0, s28
	s_lshl_b32 s49, s49, 1
	ds_read_b128 v[162:165], v226 offset:49152
	ds_read_b128 v[166:169], v226 offset:51200
	ds_read_b128 v[170:173], v227 offset:49152
	ds_read_b128 v[174:177], v227 offset:51200
	ds_read_b128 v[178:181], v226 offset:53248
	ds_read_b128 v[182:185], v226 offset:55296
	ds_read_b128 v[186:189], v227 offset:53248
	ds_read_b128 v[190:193], v227 offset:55296
	buffer_load_dwordx4 v199, s[8:11], s49 offen lds
	s_mov_b32 m0, s29
	s_or_b32 s48, s51, s48
	buffer_load_dwordx4 v205, s[8:11], s49 offen lds
	s_lshl_b32 s48, s48, 1
	s_mov_b32 m0, s30
	s_lshl_b32 s17, s17, 22
	buffer_load_dwordx4 v199, s[8:11], s48 offen lds
	s_mov_b32 m0, s31
	s_add_i32 s17, s17, s47
	buffer_load_dwordx4 v205, s[8:11], s48 offen lds
	s_mov_b32 m0, s33
	s_nop 0
	buffer_load_dwordx4 v1, s[4:7], s17 offen lds
	s_mov_b32 m0, s34
	s_nop 0
	buffer_load_dwordx4 v204, s[4:7], s17 offen lds
	v_exp_f32_e32 v244, v114
	v_exp_f32_e32 v245, v115
	v_exp_f32_e32 v246, v116
	v_exp_f32_e32 v247, v117
	v_exp_f32_e32 v248, v78
	v_exp_f32_e32 v249, v79
	v_exp_f32_e32 v250, v80
	v_exp_f32_e32 v251, v81
	v_exp_f32_e32 v252, v106
	v_exp_f32_e32 v253, v107
	v_exp_f32_e32 v254, v108
	v_exp_f32_e32 v255, v109
	v_exp_f32_e32 v232, v70
	v_exp_f32_e32 v233, v71
	v_exp_f32_e32 v234, v72
	v_exp_f32_e32 v235, v73
	s_waitcnt lgkmcnt(0)
	s_waitcnt vmcnt(8)
	s_barrier
	s_setprio 1
	s_waitcnt lgkmcnt(0)
	v_mfma_f32_16x16x32_bf16 v[90:93], v[162:165], v[130:133], v[90:93]
	v_mfma_f32_16x16x32_bf16 v[86:89], v[162:165], v[138:141], v[86:89]
	v_mfma_f32_16x16x32_bf16 v[42:45], v[166:169], v[130:133], v[42:45]
	v_mfma_f32_16x16x32_bf16 v[38:41], v[166:169], v[138:141], v[38:41]
	v_mfma_f32_16x16x32_bf16 v[126:129], v[178:181], v[130:133], v[126:129]
	v_mfma_f32_16x16x32_bf16 v[122:125], v[178:181], v[138:141], v[122:125]
	v_mfma_f32_16x16x32_bf16 v[58:61], v[182:185], v[130:133], v[58:61]
	v_mfma_f32_16x16x32_bf16 v[50:53], v[182:185], v[138:141], v[50:53]
	v_mfma_f32_16x16x32_bf16 v[90:93], v[170:173], v[134:137], v[90:93]
	v_mfma_f32_16x16x32_bf16 v[86:89], v[170:173], v[142:145], v[86:89]
	v_mfma_f32_16x16x32_bf16 v[42:45], v[174:177], v[134:137], v[42:45]
	v_mfma_f32_16x16x32_bf16 v[38:41], v[174:177], v[142:145], v[38:41]
	v_mfma_f32_16x16x32_bf16 v[126:129], v[186:189], v[134:137], v[126:129]
	v_mfma_f32_16x16x32_bf16 v[122:125], v[186:189], v[142:145], v[122:125]
	v_mfma_f32_16x16x32_bf16 v[58:61], v[190:193], v[134:137], v[58:61]
	v_mfma_f32_16x16x32_bf16 v[50:53], v[190:193], v[142:145], v[50:53]
	s_setprio 0
	s_setprio 1
	v_mfma_f32_16x16x32_bf16 v[82:85], v[162:165], v[146:149], v[82:85]
	v_mfma_f32_16x16x32_bf16 v[22:25], v[162:165], v[154:157], v[22:25]
	v_exp_f32_e32 v130, v110
	v_mfma_f32_16x16x32_bf16 v[34:37], v[166:169], v[146:149], v[34:37]
	v_exp_f32_e32 v131, v111
	v_mfma_f32_16x16x32_bf16 v[6:9], v[166:169], v[154:157], v[6:9]
	v_exp_f32_e32 v132, v112
	v_mfma_f32_16x16x32_bf16 v[118:121], v[178:181], v[146:149], v[118:121]
	v_exp_f32_e32 v133, v113
	v_mfma_f32_16x16x32_bf16 v[30:33], v[178:181], v[154:157], v[30:33]
	v_exp_f32_e32 v134, v74
	v_mfma_f32_16x16x32_bf16 v[46:49], v[182:185], v[146:149], v[46:49]
	v_exp_f32_e32 v135, v75
	v_mfma_f32_16x16x32_bf16 v[14:17], v[182:185], v[154:157], v[14:17]
	v_exp_f32_e32 v136, v76
	v_mfma_f32_16x16x32_bf16 v[82:85], v[170:173], v[150:153], v[82:85]
	v_exp_f32_e32 v137, v77
	v_mfma_f32_16x16x32_bf16 v[22:25], v[170:173], v[158:161], v[22:25]
	v_exp_f32_e32 v138, v102
	v_mfma_f32_16x16x32_bf16 v[34:37], v[174:177], v[150:153], v[34:37]
	v_exp_f32_e32 v139, v103
	v_mfma_f32_16x16x32_bf16 v[6:9], v[174:177], v[158:161], v[6:9]
	v_exp_f32_e32 v140, v104
	v_mfma_f32_16x16x32_bf16 v[118:121], v[186:189], v[150:153], v[118:121]
	v_exp_f32_e32 v141, v105
	v_mfma_f32_16x16x32_bf16 v[30:33], v[186:189], v[158:161], v[30:33]
	v_exp_f32_e32 v142, v66
	v_mfma_f32_16x16x32_bf16 v[46:49], v[190:193], v[150:153], v[46:49]
	v_exp_f32_e32 v143, v67
	v_mfma_f32_16x16x32_bf16 v[14:17], v[190:193], v[158:161], v[14:17]
	v_exp_f32_e32 v144, v68
	v_exp_f32_e32 v145, v69
	s_setprio 0
	s_barrier
.LBB3_11:
	s_lshl_b32 s58, s42, 7
	s_add_i32 s59, s41, 0x400
	s_lshr_b32 s59, s59, 6
	s_bfe_u32 s60, s20, 0x1000c
	s_add_i32 s59, s59, s60
	s_lshl_b32 s59, s59, 19
	s_add_u32 s58, s58, s59
	s_add_u32 s58, s56, s58
	s_addc_u32 s59, s57, 0
	s_add_u32 s60, s58, 0x4000
	s_addc_u32 s61, s59, 0
	s_add_u32 s62, s58, 0x100000
	s_addc_u32 s63, s59, 0
	s_add_u32 s64, s62, 0x4000
	s_addc_u32 s65, s63, 0
	s_lshr_b32 s66, s41, 7
	s_bfe_u32 s67, s20, 0x1000c
	s_add_i32 s66, s66, s67
	s_lshl_b32 s66, s66, 14
	s_lshl_b32 s67, s42, 2
	s_add_u32 s66, s66, s67
	s_add_u32 s66, s14, s66
	s_addc_u32 s67, s15, 0
	v_add_u32_e32 v172, s43, v207
	v_pk_fma_f32 v[244:245], v[244:245], -0.5, -0.5 op_sel_hi:[1,0,0]
	v_pk_fma_f32 v[246:247], v[246:247], -0.5, -0.5 op_sel_hi:[1,0,0]
	v_pk_fma_f32 v[248:249], v[248:249], -0.5, -0.5 op_sel_hi:[1,0,0]
	v_pk_fma_f32 v[250:251], v[250:251], -0.5, -0.5 op_sel_hi:[1,0,0]
	v_pk_fma_f32 v[252:253], v[252:253], -0.5, -0.5 op_sel_hi:[1,0,0]
	v_pk_fma_f32 v[254:255], v[254:255], -0.5, -0.5 op_sel_hi:[1,0,0]
	v_pk_fma_f32 v[232:233], v[232:233], -0.5, -0.5 op_sel_hi:[1,0,0]
	v_pk_fma_f32 v[234:235], v[234:235], -0.5, -0.5 op_sel_hi:[1,0,0]
	v_pk_mul_f32 v[146:147], v[244:245], v[246:247]
	v_pk_mul_f32 v[148:149], v[248:249], v[250:251]
	v_pk_mul_f32 v[150:151], v[252:253], v[254:255]
	v_pk_mul_f32 v[152:153], v[232:233], v[234:235]
	v_mul_f32_e32 v188, v146, v147
	v_mul_f32_e32 v190, v148, v149
	v_mul_f32_e32 v189, v150, v151
	v_mul_f32_e32 v191, v152, v153
	v_pk_mul_f32 v[192:193], v[188:189], v[190:191]
	v_mul_f32_e32 v162, v192, v193
	v_rcp_f32_e32 v173, v162
	v_pk_add_f32 v[164:165], v[114:115], v[116:117]
	v_pk_add_f32 v[164:165], v[164:165], v[78:79]
	v_pk_add_f32 v[164:165], v[164:165], v[80:81]
	v_pk_add_f32 v[164:165], v[164:165], v[106:107]
	v_pk_add_f32 v[164:165], v[164:165], v[108:109]
	v_pk_add_f32 v[164:165], v[164:165], v[70:71]
	v_pk_add_f32 v[164:165], v[164:165], v[72:73]
	v_pk_mul_f32 v[230:231], v[172:173], v[192:193] op_sel:[1,1] op_sel_hi:[1,0]
	v_pk_mul_f32 v[192:193], v[230:231], v[190:191]
	v_pk_mul_f32 v[190:191], v[230:231], v[188:189]
	v_pk_mul_f32 v[176:177], v[192:193], v[146:147] op_sel:[0,1] op_sel_hi:[0,0]
	v_pk_mul_f32 v[180:181], v[190:191], v[148:149] op_sel:[0,1] op_sel_hi:[0,0]
	v_pk_mul_f32 v[184:185], v[192:193], v[150:151] op_sel:[1,1] op_sel_hi:[1,0]
	v_pk_mul_f32 v[236:237], v[190:191], v[152:153] op_sel:[1,1] op_sel_hi:[1,0]
	v_pk_fma_f32 v[146:147], v[176:177], v[246:247], 1.0 op_sel_hi:[1,1,0]
	v_pk_fma_f32 v[178:179], v[176:177], v[244:245], 1.0 op_sel_hi:[1,1,0]
	v_pk_fma_f32 v[148:149], v[180:181], v[250:251], 1.0 op_sel_hi:[1,1,0]
	v_pk_fma_f32 v[182:183], v[180:181], v[248:249], 1.0 op_sel_hi:[1,1,0]
	v_pk_fma_f32 v[150:151], v[184:185], v[254:255], 1.0 op_sel_hi:[1,1,0]
	v_pk_fma_f32 v[186:187], v[184:185], v[252:253], 1.0 op_sel_hi:[1,1,0]
	v_pk_fma_f32 v[152:153], v[236:237], v[234:235], 1.0 op_sel_hi:[1,1,0]
	v_pk_fma_f32 v[238:239], v[236:237], v[232:233], 1.0 op_sel_hi:[1,1,0]
	v_cvt_pk_bf16_f32 v154, v146, v147
	v_cvt_pk_bf16_f32 v155, v178, v179
	v_cvt_pk_bf16_f32 v156, v148, v149
	v_cvt_pk_bf16_f32 v157, v182, v183
	v_cvt_pk_bf16_f32 v158, v150, v151
	v_cvt_pk_bf16_f32 v159, v186, v187
	v_cvt_pk_bf16_f32 v160, v152, v153
	v_cvt_pk_bf16_f32 v161, v238, v239
	ds_read_b128 v[114:117], v172
	ds_read_b128 v[78:81], v172 offset:64
	ds_read_b128 v[106:109], v172 offset:128
	ds_read_b128 v[70:73], v172 offset:192
	v_permlane16_swap_b32_e32 v154, v156
	v_permlane16_swap_b32_e32 v155, v157
	global_store_dwordx4 v228, v[154:157], s[58:59] nt
	s_bitcmp1_b32 s20, 12
	s_cbranch_scc1 .Lg1_noX
	s_barrier
.Lg1_noX:
	v_permlane16_swap_b32_e32 v158, v160
	v_permlane16_swap_b32_e32 v159, v161
	global_store_dwordx4 v228, v[158:161], s[58:59] offset:128 nt
	v_pk_fma_f32 v[130:131], v[130:131], -0.5, -0.5 op_sel_hi:[1,0,0]
	v_pk_fma_f32 v[132:133], v[132:133], -0.5, -0.5 op_sel_hi:[1,0,0]
	v_pk_fma_f32 v[134:135], v[134:135], -0.5, -0.5 op_sel_hi:[1,0,0]
	v_pk_fma_f32 v[136:137], v[136:137], -0.5, -0.5 op_sel_hi:[1,0,0]
	v_pk_fma_f32 v[138:139], v[138:139], -0.5, -0.5 op_sel_hi:[1,0,0]
	v_pk_fma_f32 v[140:141], v[140:141], -0.5, -0.5 op_sel_hi:[1,0,0]
	v_pk_fma_f32 v[142:143], v[142:143], -0.5, -0.5 op_sel_hi:[1,0,0]
	v_pk_fma_f32 v[144:145], v[144:145], -0.5, -0.5 op_sel_hi:[1,0,0]
	v_pk_mul_f32 v[146:147], v[130:131], v[132:133]
	v_pk_mul_f32 v[148:149], v[134:135], v[136:137]
	v_pk_mul_f32 v[150:151], v[138:139], v[140:141]
	v_pk_mul_f32 v[152:153], v[142:143], v[144:145]
	v_mul_f32_e32 v188, v146, v147
	v_mul_f32_e32 v190, v148, v149
	v_mul_f32_e32 v189, v150, v151
	v_mul_f32_e32 v191, v152, v153
	v_pk_mul_f32 v[192:193], v[188:189], v[190:191]
	v_mul_f32_e32 v244, v192, v193
	v_rcp_f32_e32 v173, v244
	v_pk_add_f32 v[246:247], v[110:111], v[112:113]
	v_pk_add_f32 v[246:247], v[246:247], v[74:75]
	v_pk_add_f32 v[246:247], v[246:247], v[76:77]
	v_pk_add_f32 v[246:247], v[246:247], v[102:103]
	v_pk_add_f32 v[246:247], v[246:247], v[104:105]
	v_pk_add_f32 v[246:247], v[246:247], v[66:67]
	v_pk_add_f32 v[246:247], v[246:247], v[68:69]
	v_pk_mul_f32 v[230:231], v[172:173], v[192:193] op_sel:[1,1] op_sel_hi:[1,0]
	v_pk_mul_f32 v[192:193], v[230:231], v[190:191]
	v_pk_mul_f32 v[190:191], v[230:231], v[188:189]
	v_pk_mul_f32 v[176:177], v[192:193], v[146:147] op_sel:[0,1] op_sel_hi:[0,0]
	v_pk_mul_f32 v[180:181], v[190:191], v[148:149] op_sel:[0,1] op_sel_hi:[0,0]
	v_pk_mul_f32 v[184:185], v[192:193], v[150:151] op_sel:[1,1] op_sel_hi:[1,0]
	v_pk_mul_f32 v[236:237], v[190:191], v[152:153] op_sel:[1,1] op_sel_hi:[1,0]
	v_pk_fma_f32 v[146:147], v[176:177], v[132:133], 1.0 op_sel_hi:[1,1,0]
	v_pk_fma_f32 v[178:179], v[176:177], v[130:131], 1.0 op_sel_hi:[1,1,0]
	v_pk_fma_f32 v[148:149], v[180:181], v[136:137], 1.0 op_sel_hi:[1,1,0]
	v_pk_fma_f32 v[182:183], v[180:181], v[134:135], 1.0 op_sel_hi:[1,1,0]
	v_pk_fma_f32 v[150:151], v[184:185], v[140:141], 1.0 op_sel_hi:[1,1,0]
	v_pk_fma_f32 v[186:187], v[184:185], v[138:139], 1.0 op_sel_hi:[1,1,0]
	v_pk_fma_f32 v[152:153], v[236:237], v[144:145], 1.0 op_sel_hi:[1,1,0]
	v_pk_fma_f32 v[238:239], v[236:237], v[142:143], 1.0 op_sel_hi:[1,1,0]
	v_cvt_pk_bf16_f32 v154, v146, v147
	v_cvt_pk_bf16_f32 v155, v178, v179
	v_cvt_pk_bf16_f32 v156, v148, v149
	v_cvt_pk_bf16_f32 v157, v182, v183
	v_cvt_pk_bf16_f32 v158, v150, v151
	v_cvt_pk_bf16_f32 v159, v186, v187
	v_cvt_pk_bf16_f32 v160, v152, v153
	v_cvt_pk_bf16_f32 v161, v238, v239
	ds_read_b128 v[110:113], v172
	ds_read_b128 v[74:77], v172 offset:64
	ds_read_b128 v[102:105], v172 offset:128
	ds_read_b128 v[66:69], v172 offset:192
	v_permlane16_swap_b32_e32 v154, v156
	v_permlane16_swap_b32_e32 v155, v157
	global_store_dwordx4 v228, v[154:157], s[58:59] offset:2048 nt
	v_permlane16_swap_b32_e32 v158, v160
	v_permlane16_swap_b32_e32 v159, v161
	global_store_dwordx4 v228, v[158:161], s[58:59] offset:2176 nt
	v_exp_f32_e32 v130, v90
	v_exp_f32_e32 v131, v91
	v_exp_f32_e32 v132, v92
	v_exp_f32_e32 v133, v93
	v_exp_f32_e32 v142, v42
	v_exp_f32_e32 v143, v43
	v_exp_f32_e32 v144, v44
	v_exp_f32_e32 v145, v45
	v_exp_f32_e32 v176, v126
	v_exp_f32_e32 v177, v127
	v_exp_f32_e32 v178, v128
	v_exp_f32_e32 v179, v129
	v_exp_f32_e32 v232, v58
	v_exp_f32_e32 v233, v59
	v_exp_f32_e32 v234, v60
	v_exp_f32_e32 v235, v61
	v_pk_fma_f32 v[130:131], v[130:131], -0.5, -0.5 op_sel_hi:[1,0,0]
	v_pk_fma_f32 v[132:133], v[132:133], -0.5, -0.5 op_sel_hi:[1,0,0]
	v_pk_fma_f32 v[142:143], v[142:143], -0.5, -0.5 op_sel_hi:[1,0,0]
	v_pk_fma_f32 v[144:145], v[144:145], -0.5, -0.5 op_sel_hi:[1,0,0]
	v_pk_fma_f32 v[176:177], v[176:177], -0.5, -0.5 op_sel_hi:[1,0,0]
	v_pk_fma_f32 v[178:179], v[178:179], -0.5, -0.5 op_sel_hi:[1,0,0]
	v_pk_fma_f32 v[232:233], v[232:233], -0.5, -0.5 op_sel_hi:[1,0,0]
	v_pk_fma_f32 v[234:235], v[234:235], -0.5, -0.5 op_sel_hi:[1,0,0]
	v_pk_mul_f32 v[134:135], v[130:131], v[132:133]
	v_pk_mul_f32 v[146:147], v[142:143], v[144:145]
	v_pk_mul_f32 v[180:181], v[176:177], v[178:179]
	v_pk_mul_f32 v[236:237], v[232:233], v[234:235]
	v_mul_f32_e32 v188, v134, v135
	v_mul_f32_e32 v190, v146, v147
	v_mul_f32_e32 v189, v180, v181
	v_mul_f32_e32 v191, v236, v237
	v_pk_mul_f32 v[192:193], v[188:189], v[190:191]
	v_mul_f32_e32 v174, v192, v193
	v_rcp_f32_e32 v173, v174
	v_pk_add_f32 v[164:165], v[164:165], v[90:91]
	v_pk_add_f32 v[164:165], v[164:165], v[92:93]
	v_pk_add_f32 v[164:165], v[164:165], v[42:43]
	v_pk_add_f32 v[164:165], v[164:165], v[44:45]
	v_pk_add_f32 v[164:165], v[164:165], v[126:127]
	v_pk_add_f32 v[164:165], v[164:165], v[128:129]
	v_pk_add_f32 v[164:165], v[164:165], v[58:59]
	v_pk_add_f32 v[164:165], v[164:165], v[60:61]
	v_pk_mul_f32 v[230:231], v[172:173], v[192:193] op_sel:[1,1] op_sel_hi:[1,0]
	v_pk_mul_f32 v[192:193], v[230:231], v[190:191]
	v_pk_mul_f32 v[190:191], v[230:231], v[188:189]
	v_pk_mul_f32 v[136:137], v[192:193], v[134:135] op_sel:[0,1] op_sel_hi:[0,0]
	v_pk_mul_f32 v[148:149], v[190:191], v[146:147] op_sel:[0,1] op_sel_hi:[0,0]
	v_pk_mul_f32 v[182:183], v[192:193], v[180:181] op_sel:[1,1] op_sel_hi:[1,0]
	v_pk_mul_f32 v[238:239], v[190:191], v[236:237] op_sel:[1,1] op_sel_hi:[1,0]
	v_pk_fma_f32 v[138:139], v[136:137], v[132:133], 1.0 op_sel_hi:[1,1,0]
	v_pk_fma_f32 v[140:141], v[136:137], v[130:131], 1.0 op_sel_hi:[1,1,0]
	v_pk_fma_f32 v[150:151], v[148:149], v[144:145], 1.0 op_sel_hi:[1,1,0]
	v_pk_fma_f32 v[152:153], v[148:149], v[142:143], 1.0 op_sel_hi:[1,1,0]
	v_pk_fma_f32 v[184:185], v[182:183], v[178:179], 1.0 op_sel_hi:[1,1,0]
	v_pk_fma_f32 v[186:187], v[182:183], v[176:177], 1.0 op_sel_hi:[1,1,0]
	v_pk_fma_f32 v[240:241], v[238:239], v[234:235], 1.0 op_sel_hi:[1,1,0]
	v_pk_fma_f32 v[242:243], v[238:239], v[232:233], 1.0 op_sel_hi:[1,1,0]
	v_cvt_pk_bf16_f32 v154, v138, v139
	v_cvt_pk_bf16_f32 v155, v140, v141
	v_cvt_pk_bf16_f32 v156, v150, v151
	v_cvt_pk_bf16_f32 v157, v152, v153
	v_cvt_pk_bf16_f32 v158, v184, v185
	v_cvt_pk_bf16_f32 v159, v186, v187
	v_cvt_pk_bf16_f32 v160, v240, v241
	v_cvt_pk_bf16_f32 v161, v242, v243
	ds_read_b128 v[90:93], v172 offset:512
	ds_read_b128 v[42:45], v172 offset:576
	ds_read_b128 v[126:129], v172 offset:640
	ds_read_b128 v[58:61], v172 offset:704
	v_permlane16_swap_b32_e32 v154, v156
	v_permlane16_swap_b32_e32 v155, v157
	global_store_dwordx4 v228, v[154:157], s[62:63] nt
	v_permlane16_swap_b32_e32 v158, v160
	v_permlane16_swap_b32_e32 v159, v161
	global_store_dwordx4 v228, v[158:161], s[62:63] offset:128 nt
	v_log_f32_e32 v166, v162
	v_log_f32_e32 v170, v174
	v_add_f32_e32 v168, v164, v165
	v_mul_f32_e32 v168, 0xbeb17218, v168
	v_add_f32_e32 v166, v166, v170
	v_fmac_f32_e32 v168, 0x3f317218, v166
	v_mov_b32_e32 v169, v168
	s_nop 1
	v_permlane16_swap_b32_e32 v168, v169
	v_add_f32_e32 v168, v168, v169
	v_mov_b32_e32 v169, v168
	s_nop 1
	v_permlane32_swap_b32_e32 v168, v169
	v_add_f32_e32 v168, v168, v169
	s_mov_b64 exec, s[0:1]
	global_store_dword v229, v168, s[66:67]
	s_mov_b64 exec, -1
	v_exp_f32_e32 v130, v86
	v_exp_f32_e32 v131, v87
	v_exp_f32_e32 v132, v88
	v_exp_f32_e32 v133, v89
	v_exp_f32_e32 v142, v38
	v_exp_f32_e32 v143, v39
	v_exp_f32_e32 v144, v40
	v_exp_f32_e32 v145, v41
	v_exp_f32_e32 v176, v122
	v_exp_f32_e32 v177, v123
	v_exp_f32_e32 v178, v124
	v_exp_f32_e32 v179, v125
	v_exp_f32_e32 v232, v50
	v_exp_f32_e32 v233, v51
	v_exp_f32_e32 v234, v52
	v_exp_f32_e32 v235, v53
	v_pk_fma_f32 v[130:131], v[130:131], -0.5, -0.5 op_sel_hi:[1,0,0]
	v_pk_fma_f32 v[132:133], v[132:133], -0.5, -0.5 op_sel_hi:[1,0,0]
	v_pk_fma_f32 v[142:143], v[142:143], -0.5, -0.5 op_sel_hi:[1,0,0]
	v_pk_fma_f32 v[144:145], v[144:145], -0.5, -0.5 op_sel_hi:[1,0,0]
	v_pk_fma_f32 v[176:177], v[176:177], -0.5, -0.5 op_sel_hi:[1,0,0]
	v_pk_fma_f32 v[178:179], v[178:179], -0.5, -0.5 op_sel_hi:[1,0,0]
	v_pk_fma_f32 v[232:233], v[232:233], -0.5, -0.5 op_sel_hi:[1,0,0]
	v_pk_fma_f32 v[234:235], v[234:235], -0.5, -0.5 op_sel_hi:[1,0,0]
	v_pk_mul_f32 v[134:135], v[130:131], v[132:133]
	v_pk_mul_f32 v[146:147], v[142:143], v[144:145]
	v_pk_mul_f32 v[180:181], v[176:177], v[178:179]
	v_pk_mul_f32 v[236:237], v[232:233], v[234:235]
	v_mul_f32_e32 v188, v134, v135
	v_mul_f32_e32 v190, v146, v147
	v_mul_f32_e32 v189, v180, v181
	v_mul_f32_e32 v191, v236, v237
	v_pk_mul_f32 v[192:193], v[188:189], v[190:191]
	v_mul_f32_e32 v245, v192, v193
	v_rcp_f32_e32 v173, v245
	v_pk_add_f32 v[246:247], v[246:247], v[86:87]
	v_pk_add_f32 v[246:247], v[246:247], v[88:89]
	v_pk_add_f32 v[246:247], v[246:247], v[38:39]
	v_pk_add_f32 v[246:247], v[246:247], v[40:41]
	v_pk_add_f32 v[246:247], v[246:247], v[122:123]
	v_pk_add_f32 v[246:247], v[246:247], v[124:125]
	v_pk_add_f32 v[246:247], v[246:247], v[50:51]
	v_pk_add_f32 v[246:247], v[246:247], v[52:53]
	v_pk_mul_f32 v[230:231], v[172:173], v[192:193] op_sel:[1,1] op_sel_hi:[1,0]
	v_pk_mul_f32 v[192:193], v[230:231], v[190:191]
	v_pk_mul_f32 v[190:191], v[230:231], v[188:189]
	v_pk_mul_f32 v[136:137], v[192:193], v[134:135] op_sel:[0,1] op_sel_hi:[0,0]
	v_pk_mul_f32 v[148:149], v[190:191], v[146:147] op_sel:[0,1] op_sel_hi:[0,0]
	v_pk_mul_f32 v[182:183], v[192:193], v[180:181] op_sel:[1,1] op_sel_hi:[1,0]
	v_pk_mul_f32 v[238:239], v[190:191], v[236:237] op_sel:[1,1] op_sel_hi:[1,0]
	v_pk_fma_f32 v[138:139], v[136:137], v[132:133], 1.0 op_sel_hi:[1,1,0]
	v_pk_fma_f32 v[140:141], v[136:137], v[130:131], 1.0 op_sel_hi:[1,1,0]
	v_pk_fma_f32 v[150:151], v[148:149], v[144:145], 1.0 op_sel_hi:[1,1,0]
	v_pk_fma_f32 v[152:153], v[148:149], v[142:143], 1.0 op_sel_hi:[1,1,0]
	v_pk_fma_f32 v[184:185], v[182:183], v[178:179], 1.0 op_sel_hi:[1,1,0]
	v_pk_fma_f32 v[186:187], v[182:183], v[176:177], 1.0 op_sel_hi:[1,1,0]
	v_pk_fma_f32 v[240:241], v[238:239], v[234:235], 1.0 op_sel_hi:[1,1,0]
	v_pk_fma_f32 v[242:243], v[238:239], v[232:233], 1.0 op_sel_hi:[1,1,0]
	v_cvt_pk_bf16_f32 v154, v138, v139
	v_cvt_pk_bf16_f32 v155, v140, v141
	v_cvt_pk_bf16_f32 v156, v150, v151
	v_cvt_pk_bf16_f32 v157, v152, v153
	v_cvt_pk_bf16_f32 v158, v184, v185
	v_cvt_pk_bf16_f32 v159, v186, v187
	v_cvt_pk_bf16_f32 v160, v240, v241
	v_cvt_pk_bf16_f32 v161, v242, v243
	ds_read_b128 v[86:89], v172 offset:512
	ds_read_b128 v[38:41], v172 offset:576
	ds_read_b128 v[122:125], v172 offset:640
	ds_read_b128 v[50:53], v172 offset:704
	v_permlane16_swap_b32_e32 v154, v156
	v_permlane16_swap_b32_e32 v155, v157
	global_store_dwordx4 v228, v[154:157], s[62:63] offset:2048 nt
	v_permlane16_swap_b32_e32 v158, v160
	v_permlane16_swap_b32_e32 v159, v161
	global_store_dwordx4 v228, v[158:161], s[62:63] offset:2176 nt
	v_log_f32_e32 v166, v244
	v_log_f32_e32 v170, v245
	v_add_f32_e32 v168, v246, v247
	v_mul_f32_e32 v168, 0xbeb17218, v168
	v_add_f32_e32 v166, v166, v170
	v_fmac_f32_e32 v168, 0x3f317218, v166
	v_mov_b32_e32 v169, v168
	s_nop 1
	v_permlane16_swap_b32_e32 v168, v169
	v_add_f32_e32 v168, v168, v169
	v_mov_b32_e32 v169, v168
	s_nop 1
	v_permlane32_swap_b32_e32 v168, v169
	v_add_f32_e32 v168, v168, v169
	s_mov_b64 exec, s[0:1]
	global_store_dword v229, v168, s[66:67] offset:64
	s_mov_b64 exec, -1
	v_exp_f32_e32 v130, v98
	v_exp_f32_e32 v131, v99
	v_exp_f32_e32 v132, v100
	v_exp_f32_e32 v133, v101
	v_exp_f32_e32 v142, v62
	v_exp_f32_e32 v143, v63
	v_exp_f32_e32 v144, v64
	v_exp_f32_e32 v145, v65
	v_exp_f32_e32 v176, v94
	v_exp_f32_e32 v177, v95
	v_exp_f32_e32 v178, v96
	v_exp_f32_e32 v179, v97
	v_exp_f32_e32 v232, v54
	v_exp_f32_e32 v233, v55
	v_exp_f32_e32 v234, v56
	v_exp_f32_e32 v235, v57
	v_pk_fma_f32 v[130:131], v[130:131], -0.5, -0.5 op_sel_hi:[1,0,0]
	v_pk_fma_f32 v[132:133], v[132:133], -0.5, -0.5 op_sel_hi:[1,0,0]
	v_pk_fma_f32 v[142:143], v[142:143], -0.5, -0.5 op_sel_hi:[1,0,0]
	v_pk_fma_f32 v[144:145], v[144:145], -0.5, -0.5 op_sel_hi:[1,0,0]
	v_pk_fma_f32 v[176:177], v[176:177], -0.5, -0.5 op_sel_hi:[1,0,0]
	v_pk_fma_f32 v[178:179], v[178:179], -0.5, -0.5 op_sel_hi:[1,0,0]
	v_pk_fma_f32 v[232:233], v[232:233], -0.5, -0.5 op_sel_hi:[1,0,0]
	v_pk_fma_f32 v[234:235], v[234:235], -0.5, -0.5 op_sel_hi:[1,0,0]
	v_pk_mul_f32 v[134:135], v[130:131], v[132:133]
	v_pk_mul_f32 v[146:147], v[142:143], v[144:145]
	v_pk_mul_f32 v[180:181], v[176:177], v[178:179]
	v_pk_mul_f32 v[236:237], v[232:233], v[234:235]
	v_mul_f32_e32 v188, v134, v135
	v_mul_f32_e32 v190, v146, v147
	v_mul_f32_e32 v189, v180, v181
	v_mul_f32_e32 v191, v236, v237
	v_pk_mul_f32 v[192:193], v[188:189], v[190:191]
	v_mul_f32_e32 v162, v192, v193
	v_rcp_f32_e32 v173, v162
	v_pk_add_f32 v[164:165], v[98:99], v[100:101]
	v_pk_add_f32 v[164:165], v[164:165], v[62:63]
	v_pk_add_f32 v[164:165], v[164:165], v[64:65]
	v_pk_add_f32 v[164:165], v[164:165], v[94:95]
	v_pk_add_f32 v[164:165], v[164:165], v[96:97]
	v_pk_add_f32 v[164:165], v[164:165], v[54:55]
	v_pk_add_f32 v[164:165], v[164:165], v[56:57]
	v_pk_mul_f32 v[230:231], v[172:173], v[192:193] op_sel:[1,1] op_sel_hi:[1,0]
	v_pk_mul_f32 v[192:193], v[230:231], v[190:191]
	v_pk_mul_f32 v[190:191], v[230:231], v[188:189]
	v_pk_mul_f32 v[136:137], v[192:193], v[134:135] op_sel:[0,1] op_sel_hi:[0,0]
	v_pk_mul_f32 v[148:149], v[190:191], v[146:147] op_sel:[0,1] op_sel_hi:[0,0]
	v_pk_mul_f32 v[182:183], v[192:193], v[180:181] op_sel:[1,1] op_sel_hi:[1,0]
	v_pk_mul_f32 v[238:239], v[190:191], v[236:237] op_sel:[1,1] op_sel_hi:[1,0]
	v_pk_fma_f32 v[138:139], v[136:137], v[132:133], 1.0 op_sel_hi:[1,1,0]
	v_pk_fma_f32 v[140:141], v[136:137], v[130:131], 1.0 op_sel_hi:[1,1,0]
	v_pk_fma_f32 v[150:151], v[148:149], v[144:145], 1.0 op_sel_hi:[1,1,0]
	v_pk_fma_f32 v[152:153], v[148:149], v[142:143], 1.0 op_sel_hi:[1,1,0]
	v_pk_fma_f32 v[184:185], v[182:183], v[178:179], 1.0 op_sel_hi:[1,1,0]
	v_pk_fma_f32 v[186:187], v[182:183], v[176:177], 1.0 op_sel_hi:[1,1,0]
	v_pk_fma_f32 v[240:241], v[238:239], v[234:235], 1.0 op_sel_hi:[1,1,0]
	v_pk_fma_f32 v[242:243], v[238:239], v[232:233], 1.0 op_sel_hi:[1,1,0]
	v_cvt_pk_bf16_f32 v154, v138, v139
	v_cvt_pk_bf16_f32 v155, v140, v141
	v_cvt_pk_bf16_f32 v156, v150, v151
	v_cvt_pk_bf16_f32 v157, v152, v153
	v_cvt_pk_bf16_f32 v158, v184, v185
	v_cvt_pk_bf16_f32 v159, v186, v187
	v_cvt_pk_bf16_f32 v160, v240, v241
	v_cvt_pk_bf16_f32 v161, v242, v243
	ds_read_b128 v[98:101], v172
	ds_read_b128 v[62:65], v172 offset:64
	ds_read_b128 v[94:97], v172 offset:128
	ds_read_b128 v[54:57], v172 offset:192
	v_permlane16_swap_b32_e32 v154, v156
	v_permlane16_swap_b32_e32 v155, v157
	global_store_dwordx4 v228, v[154:157], s[60:61] nt
	v_permlane16_swap_b32_e32 v158, v160
	v_permlane16_swap_b32_e32 v159, v161
	global_store_dwordx4 v228, v[158:161], s[60:61] offset:128 nt
	v_exp_f32_e32 v130, v82
	v_exp_f32_e32 v131, v83
	v_exp_f32_e32 v132, v84
	v_exp_f32_e32 v133, v85
	v_exp_f32_e32 v142, v34
	v_exp_f32_e32 v143, v35
	v_exp_f32_e32 v144, v36
	v_exp_f32_e32 v145, v37
	v_exp_f32_e32 v176, v118
	v_exp_f32_e32 v177, v119
	v_exp_f32_e32 v178, v120
	v_exp_f32_e32 v179, v121
	v_exp_f32_e32 v232, v46
	v_exp_f32_e32 v233, v47
	v_exp_f32_e32 v234, v48
	v_exp_f32_e32 v235, v49
	v_pk_fma_f32 v[130:131], v[130:131], -0.5, -0.5 op_sel_hi:[1,0,0]
	v_pk_fma_f32 v[132:133], v[132:133], -0.5, -0.5 op_sel_hi:[1,0,0]
	v_pk_fma_f32 v[142:143], v[142:143], -0.5, -0.5 op_sel_hi:[1,0,0]
	v_pk_fma_f32 v[144:145], v[144:145], -0.5, -0.5 op_sel_hi:[1,0,0]
	v_pk_fma_f32 v[176:177], v[176:177], -0.5, -0.5 op_sel_hi:[1,0,0]
	v_pk_fma_f32 v[178:179], v[178:179], -0.5, -0.5 op_sel_hi:[1,0,0]
	v_pk_fma_f32 v[232:233], v[232:233], -0.5, -0.5 op_sel_hi:[1,0,0]
	v_pk_fma_f32 v[234:235], v[234:235], -0.5, -0.5 op_sel_hi:[1,0,0]
	v_pk_mul_f32 v[134:135], v[130:131], v[132:133]
	v_pk_mul_f32 v[146:147], v[142:143], v[144:145]
	v_pk_mul_f32 v[180:181], v[176:177], v[178:179]
	v_pk_mul_f32 v[236:237], v[232:233], v[234:235]
	v_mul_f32_e32 v188, v134, v135
	v_mul_f32_e32 v190, v146, v147
	v_mul_f32_e32 v189, v180, v181
	v_mul_f32_e32 v191, v236, v237
	v_pk_mul_f32 v[192:193], v[188:189], v[190:191]
	v_mul_f32_e32 v174, v192, v193
	v_rcp_f32_e32 v173, v174
	v_pk_add_f32 v[164:165], v[164:165], v[82:83]
	v_pk_add_f32 v[164:165], v[164:165], v[84:85]
	v_pk_add_f32 v[164:165], v[164:165], v[34:35]
	v_pk_add_f32 v[164:165], v[164:165], v[36:37]
	v_pk_add_f32 v[164:165], v[164:165], v[118:119]
	v_pk_add_f32 v[164:165], v[164:165], v[120:121]
	v_pk_add_f32 v[164:165], v[164:165], v[46:47]
	v_pk_add_f32 v[164:165], v[164:165], v[48:49]
	v_pk_mul_f32 v[230:231], v[172:173], v[192:193] op_sel:[1,1] op_sel_hi:[1,0]
	v_pk_mul_f32 v[192:193], v[230:231], v[190:191]
	v_pk_mul_f32 v[190:191], v[230:231], v[188:189]
	v_pk_mul_f32 v[136:137], v[192:193], v[134:135] op_sel:[0,1] op_sel_hi:[0,0]
	v_pk_mul_f32 v[148:149], v[190:191], v[146:147] op_sel:[0,1] op_sel_hi:[0,0]
	v_pk_mul_f32 v[182:183], v[192:193], v[180:181] op_sel:[1,1] op_sel_hi:[1,0]
	v_pk_mul_f32 v[238:239], v[190:191], v[236:237] op_sel:[1,1] op_sel_hi:[1,0]
	v_pk_fma_f32 v[138:139], v[136:137], v[132:133], 1.0 op_sel_hi:[1,1,0]
	v_pk_fma_f32 v[140:141], v[136:137], v[130:131], 1.0 op_sel_hi:[1,1,0]
	v_pk_fma_f32 v[150:151], v[148:149], v[144:145], 1.0 op_sel_hi:[1,1,0]
	v_pk_fma_f32 v[152:153], v[148:149], v[142:143], 1.0 op_sel_hi:[1,1,0]
	v_pk_fma_f32 v[184:185], v[182:183], v[178:179], 1.0 op_sel_hi:[1,1,0]
	v_pk_fma_f32 v[186:187], v[182:183], v[176:177], 1.0 op_sel_hi:[1,1,0]
	v_pk_fma_f32 v[240:241], v[238:239], v[234:235], 1.0 op_sel_hi:[1,1,0]
	v_pk_fma_f32 v[242:243], v[238:239], v[232:233], 1.0 op_sel_hi:[1,1,0]
	v_cvt_pk_bf16_f32 v154, v138, v139
	v_cvt_pk_bf16_f32 v155, v140, v141
	v_cvt_pk_bf16_f32 v156, v150, v151
	v_cvt_pk_bf16_f32 v157, v152, v153
	v_cvt_pk_bf16_f32 v158, v184, v185
	v_cvt_pk_bf16_f32 v159, v186, v187
	v_cvt_pk_bf16_f32 v160, v240, v241
	v_cvt_pk_bf16_f32 v161, v242, v243
	ds_read_b128 v[82:85], v172 offset:512
	ds_read_b128 v[34:37], v172 offset:576
	ds_read_b128 v[118:121], v172 offset:640
	ds_read_b128 v[46:49], v172 offset:704
	v_permlane16_swap_b32_e32 v154, v156
	v_permlane16_swap_b32_e32 v155, v157
	global_store_dwordx4 v228, v[154:157], s[64:65] nt
	v_permlane16_swap_b32_e32 v158, v160
	v_permlane16_swap_b32_e32 v159, v161
	global_store_dwordx4 v228, v[158:161], s[64:65] offset:128 nt
	v_log_f32_e32 v166, v162
	v_log_f32_e32 v170, v174
	v_add_f32_e32 v168, v164, v165
	v_mul_f32_e32 v168, 0xbeb17218, v168
	v_add_f32_e32 v166, v166, v170
	v_fmac_f32_e32 v168, 0x3f317218, v166
	v_mov_b32_e32 v169, v168
	s_nop 1
	v_permlane16_swap_b32_e32 v168, v169
	v_add_f32_e32 v168, v168, v169
	v_mov_b32_e32 v169, v168
	s_nop 1
	v_permlane32_swap_b32_e32 v168, v169
	v_add_f32_e32 v168, v168, v169
	s_mov_b64 exec, s[0:1]
	global_store_dword v229, v168, s[66:67] offset:512
	s_mov_b64 exec, -1
	v_exp_f32_e32 v130, v18
	v_exp_f32_e32 v131, v19
	v_exp_f32_e32 v132, v20
	v_exp_f32_e32 v133, v21
	v_exp_f32_e32 v142, v2
	v_exp_f32_e32 v143, v3
	v_exp_f32_e32 v144, v4
	v_exp_f32_e32 v145, v5
	v_exp_f32_e32 v176, v26
	v_exp_f32_e32 v177, v27
	v_exp_f32_e32 v178, v28
	v_exp_f32_e32 v179, v29
	v_exp_f32_e32 v232, v10
	v_exp_f32_e32 v233, v11
	v_exp_f32_e32 v234, v12
	v_exp_f32_e32 v235, v13
	v_pk_fma_f32 v[130:131], v[130:131], -0.5, -0.5 op_sel_hi:[1,0,0]
	v_pk_fma_f32 v[132:133], v[132:133], -0.5, -0.5 op_sel_hi:[1,0,0]
	v_pk_fma_f32 v[142:143], v[142:143], -0.5, -0.5 op_sel_hi:[1,0,0]
	v_pk_fma_f32 v[144:145], v[144:145], -0.5, -0.5 op_sel_hi:[1,0,0]
	v_pk_fma_f32 v[176:177], v[176:177], -0.5, -0.5 op_sel_hi:[1,0,0]
	v_pk_fma_f32 v[178:179], v[178:179], -0.5, -0.5 op_sel_hi:[1,0,0]
	v_pk_fma_f32 v[232:233], v[232:233], -0.5, -0.5 op_sel_hi:[1,0,0]
	v_pk_fma_f32 v[234:235], v[234:235], -0.5, -0.5 op_sel_hi:[1,0,0]
	v_pk_mul_f32 v[134:135], v[130:131], v[132:133]
	v_pk_mul_f32 v[146:147], v[142:143], v[144:145]
	v_pk_mul_f32 v[180:181], v[176:177], v[178:179]
	v_pk_mul_f32 v[236:237], v[232:233], v[234:235]
	v_mul_f32_e32 v188, v134, v135
	v_mul_f32_e32 v190, v146, v147
	v_mul_f32_e32 v189, v180, v181
	v_mul_f32_e32 v191, v236, v237
	v_pk_mul_f32 v[192:193], v[188:189], v[190:191]
	v_mul_f32_e32 v162, v192, v193
	v_rcp_f32_e32 v173, v162
	v_pk_add_f32 v[164:165], v[18:19], v[20:21]
	v_pk_add_f32 v[164:165], v[164:165], v[2:3]
	v_pk_add_f32 v[164:165], v[164:165], v[4:5]
	v_pk_add_f32 v[164:165], v[164:165], v[26:27]
	v_pk_add_f32 v[164:165], v[164:165], v[28:29]
	v_pk_add_f32 v[164:165], v[164:165], v[10:11]
	v_pk_add_f32 v[164:165], v[164:165], v[12:13]
	v_pk_mul_f32 v[230:231], v[172:173], v[192:193] op_sel:[1,1] op_sel_hi:[1,0]
	v_pk_mul_f32 v[192:193], v[230:231], v[190:191]
	v_pk_mul_f32 v[190:191], v[230:231], v[188:189]
	v_pk_mul_f32 v[136:137], v[192:193], v[134:135] op_sel:[0,1] op_sel_hi:[0,0]
	v_pk_mul_f32 v[148:149], v[190:191], v[146:147] op_sel:[0,1] op_sel_hi:[0,0]
	v_pk_mul_f32 v[182:183], v[192:193], v[180:181] op_sel:[1,1] op_sel_hi:[1,0]
	v_pk_mul_f32 v[238:239], v[190:191], v[236:237] op_sel:[1,1] op_sel_hi:[1,0]
	v_pk_fma_f32 v[138:139], v[136:137], v[132:133], 1.0 op_sel_hi:[1,1,0]
	v_pk_fma_f32 v[140:141], v[136:137], v[130:131], 1.0 op_sel_hi:[1,1,0]
	v_pk_fma_f32 v[150:151], v[148:149], v[144:145], 1.0 op_sel_hi:[1,1,0]
	v_pk_fma_f32 v[152:153], v[148:149], v[142:143], 1.0 op_sel_hi:[1,1,0]
	v_pk_fma_f32 v[184:185], v[182:183], v[178:179], 1.0 op_sel_hi:[1,1,0]
	v_pk_fma_f32 v[186:187], v[182:183], v[176:177], 1.0 op_sel_hi:[1,1,0]
	v_pk_fma_f32 v[240:241], v[238:239], v[234:235], 1.0 op_sel_hi:[1,1,0]
	v_pk_fma_f32 v[242:243], v[238:239], v[232:233], 1.0 op_sel_hi:[1,1,0]
	v_cvt_pk_bf16_f32 v154, v138, v139
	v_cvt_pk_bf16_f32 v155, v140, v141
	v_cvt_pk_bf16_f32 v156, v150, v151
	v_cvt_pk_bf16_f32 v157, v152, v153
	v_cvt_pk_bf16_f32 v158, v184, v185
	v_cvt_pk_bf16_f32 v159, v186, v187
	v_cvt_pk_bf16_f32 v160, v240, v241
	v_cvt_pk_bf16_f32 v161, v242, v243
	ds_read_b128 v[18:21], v172
	ds_read_b128 v[2:5], v172 offset:64
	ds_read_b128 v[26:29], v172 offset:128
	ds_read_b128 v[10:13], v172 offset:192
	v_permlane16_swap_b32_e32 v154, v156
	v_permlane16_swap_b32_e32 v155, v157
	global_store_dwordx4 v228, v[154:157], s[60:61] offset:2048 nt
	v_permlane16_swap_b32_e32 v158, v160
	v_permlane16_swap_b32_e32 v159, v161
	global_store_dwordx4 v228, v[158:161], s[60:61] offset:2176 nt
	v_exp_f32_e32 v130, v22
	v_exp_f32_e32 v131, v23
	v_exp_f32_e32 v132, v24
	v_exp_f32_e32 v133, v25
	v_exp_f32_e32 v142, v6
	v_exp_f32_e32 v143, v7
	v_exp_f32_e32 v144, v8
	v_exp_f32_e32 v145, v9
	v_exp_f32_e32 v176, v30
	v_exp_f32_e32 v177, v31
	v_exp_f32_e32 v178, v32
	v_exp_f32_e32 v179, v33
	v_exp_f32_e32 v232, v14
	v_exp_f32_e32 v233, v15
	v_exp_f32_e32 v234, v16
	v_exp_f32_e32 v235, v17
	v_pk_fma_f32 v[130:131], v[130:131], -0.5, -0.5 op_sel_hi:[1,0,0]
	v_pk_fma_f32 v[132:133], v[132:133], -0.5, -0.5 op_sel_hi:[1,0,0]
	v_pk_fma_f32 v[142:143], v[142:143], -0.5, -0.5 op_sel_hi:[1,0,0]
	v_pk_fma_f32 v[144:145], v[144:145], -0.5, -0.5 op_sel_hi:[1,0,0]
	v_pk_fma_f32 v[176:177], v[176:177], -0.5, -0.5 op_sel_hi:[1,0,0]
	v_pk_fma_f32 v[178:179], v[178:179], -0.5, -0.5 op_sel_hi:[1,0,0]
	v_pk_fma_f32 v[232:233], v[232:233], -0.5, -0.5 op_sel_hi:[1,0,0]
	v_pk_fma_f32 v[234:235], v[234:235], -0.5, -0.5 op_sel_hi:[1,0,0]
	v_pk_mul_f32 v[134:135], v[130:131], v[132:133]
	v_pk_mul_f32 v[146:147], v[142:143], v[144:145]
	v_pk_mul_f32 v[180:181], v[176:177], v[178:179]
	v_pk_mul_f32 v[236:237], v[232:233], v[234:235]
	v_mul_f32_e32 v188, v134, v135
	v_mul_f32_e32 v190, v146, v147
	v_mul_f32_e32 v189, v180, v181
	v_mul_f32_e32 v191, v236, v237
	v_pk_mul_f32 v[192:193], v[188:189], v[190:191]
	v_mul_f32_e32 v174, v192, v193
	v_rcp_f32_e32 v173, v174
	v_pk_add_f32 v[164:165], v[164:165], v[22:23]
	v_pk_add_f32 v[164:165], v[164:165], v[24:25]
	v_pk_add_f32 v[164:165], v[164:165], v[6:7]
	v_pk_add_f32 v[164:165], v[164:165], v[8:9]
	v_pk_add_f32 v[164:165], v[164:165], v[30:31]
	v_pk_add_f32 v[164:165], v[164:165], v[32:33]
	v_pk_add_f32 v[164:165], v[164:165], v[14:15]
	v_pk_add_f32 v[164:165], v[164:165], v[16:17]
	v_pk_mul_f32 v[230:231], v[172:173], v[192:193] op_sel:[1,1] op_sel_hi:[1,0]
	v_pk_mul_f32 v[192:193], v[230:231], v[190:191]
	v_pk_mul_f32 v[190:191], v[230:231], v[188:189]
	v_pk_mul_f32 v[136:137], v[192:193], v[134:135] op_sel:[0,1] op_sel_hi:[0,0]
	v_pk_mul_f32 v[148:149], v[190:191], v[146:147] op_sel:[0,1] op_sel_hi:[0,0]
	v_pk_mul_f32 v[182:183], v[192:193], v[180:181] op_sel:[1,1] op_sel_hi:[1,0]
	v_pk_mul_f32 v[238:239], v[190:191], v[236:237] op_sel:[1,1] op_sel_hi:[1,0]
	v_pk_fma_f32 v[138:139], v[136:137], v[132:133], 1.0 op_sel_hi:[1,1,0]
	v_pk_fma_f32 v[140:141], v[136:137], v[130:131], 1.0 op_sel_hi:[1,1,0]
	v_pk_fma_f32 v[150:151], v[148:149], v[144:145], 1.0 op_sel_hi:[1,1,0]
	v_pk_fma_f32 v[152:153], v[148:149], v[142:143], 1.0 op_sel_hi:[1,1,0]
	v_pk_fma_f32 v[184:185], v[182:183], v[178:179], 1.0 op_sel_hi:[1,1,0]
	v_pk_fma_f32 v[186:187], v[182:183], v[176:177], 1.0 op_sel_hi:[1,1,0]
	v_pk_fma_f32 v[240:241], v[238:239], v[234:235], 1.0 op_sel_hi:[1,1,0]
	v_pk_fma_f32 v[242:243], v[238:239], v[232:233], 1.0 op_sel_hi:[1,1,0]
	v_cvt_pk_bf16_f32 v154, v138, v139
	v_cvt_pk_bf16_f32 v155, v140, v141
	v_cvt_pk_bf16_f32 v156, v150, v151
	v_cvt_pk_bf16_f32 v157, v152, v153
	v_cvt_pk_bf16_f32 v158, v184, v185
	v_cvt_pk_bf16_f32 v159, v186, v187
	v_cvt_pk_bf16_f32 v160, v240, v241
	v_cvt_pk_bf16_f32 v161, v242, v243
	ds_read_b128 v[22:25], v172 offset:512
	ds_read_b128 v[6:9], v172 offset:576
	ds_read_b128 v[30:33], v172 offset:640
	ds_read_b128 v[14:17], v172 offset:704
	v_permlane16_swap_b32_e32 v154, v156
	v_permlane16_swap_b32_e32 v155, v157
	global_store_dwordx4 v228, v[154:157], s[64:65] offset:2048 nt
	v_permlane16_swap_b32_e32 v158, v160
	v_permlane16_swap_b32_e32 v159, v161
	global_store_dwordx4 v228, v[158:161], s[64:65] offset:2176 nt
	v_log_f32_e32 v166, v162
	v_log_f32_e32 v170, v174
	v_add_f32_e32 v168, v164, v165
	v_mul_f32_e32 v168, 0xbeb17218, v168
	v_add_f32_e32 v166, v166, v170
	v_fmac_f32_e32 v168, 0x3f317218, v166
	v_mov_b32_e32 v169, v168
	s_nop 1
	v_permlane16_swap_b32_e32 v168, v169
	v_add_f32_e32 v168, v168, v169
	v_mov_b32_e32 v169, v168
	s_nop 1
	v_permlane32_swap_b32_e32 v168, v169
	v_add_f32_e32 v168, v168, v169
	s_mov_b64 exec, s[0:1]
	global_store_dword v229, v168, s[66:67] offset:576
	s_mov_b64 exec, -1
	s_bitcmp1_b32 s20, 12
	s_cbranch_scc0 .Lg1_noY
	s_barrier
